# v55 + in-proj tile order permuted so that the workgroups running five units (the critical ones) get the cheap-epilogue tiles (rope, plain, sigmoid) and the four-unit workgroups the gelu / LayerNorm-st
# baseline (speedup 1.0000x reference)
;     __device__ bool next(int i, Unit& u) const { if (!base.next(i >> 1, u)) return false; if (i & 1) { u.pm += MTOK / BM; u.pn += DM / BM; } return true; }
;   __device__ __forceinline__ bool next(int i,AttnUnit&u)const{ if(i>=2||vcu>=256)return false; const int s=vcu&3; u.bh=vcu>>2; u.qb=(i==0)?7-s:s; return true; }
;     __host__ __device__ bool next(int i, Unit& u) const {
;         const int L = i * G + c; if (L >= nwg) return false;
;         int wgid = L; { const int q = nwg / NXCD, r = nwg % NXCD, xcd = wgid % NXCD, off = wgid / NXCD; wgid = (xcd < r ? xcd * (q + 1) : r * (q + 1) + (xcd - r) * q) + off; }
;         const int nig = WGM * nN, gid = wgid / nig, fm = gid * WGM, gsz = (nM - fm) < WGM ? (nM - fm) : WGM;
;         u.pm = fm + ((wgid % nig) % gsz); u.pn = (wgid % nig) / gsz; u.half = 0; return true;
.LBB0_382:
	s_ashr_i32 s4, s21, 31
	s_lshr_b32 s4, s4, 29
	s_add_i32 s4, s21, s4
	s_ashr_i32 s5, s4, 3
	s_and_b32 s4, s4, -8
	s_sub_i32 s4, s21, s4
	s_cmp_lt_i32 s4, 0
	s_movk_i32 s6, 0x91
	s_cselect_b32 s6, s6, 0x90
	s_mul_i32 s4, s4, s6
	s_add_i32 s4, s4, s5
	s_mul_hi_i32 s5, s4, 0x38e38e39
	s_lshr_b32 s6, s5, 31
	s_ashr_i32 s5, s5, 5
	s_add_i32 s5, s5, s6
	s_lshl_b32 s6, s5, 3
	s_mulk_i32 s5, 0x90
	s_sub_i32 s4, s4, s5
	s_bfe_u32 s5, s4, 0x3001c
	s_add_i32 s5, s4, s5
	s_sext_i32_i16 s7, s5
	s_and_b32 s5, s5, 0xfff8
	s_sub_i32 s4, s4, s5
	s_sext_i32_i16 s4, s4
	s_add_i32 s18, s6, s4
	s_ashr_i32 s70, s7, 3
	s_mul_i32 s4, s70, 5
	s_cmp_lt_u32 s70, 12
	s_cbranch_scc0 .Lpn_hi0
	s_mov_b32 s6, 0x8e5080c4
	s_mov_b32 s7, 0x8392818
	s_branch .Lpn_go0
.Lpn_hi0:
	s_sub_i32 s4, s4, 60
	s_mov_b32 s6, 0x1ab8bd8a
	s_mov_b32 s7, 0
.Lpn_go0:
	s_lshr_b64 s[6:7], s[6:7], s4
	s_and_b32 s70, s6, 31
	s_add_u32 s22, s16, 0x800000
	s_addc_u32 s23, s17, 0
	s_andn2_b64 vcc, exec, s[0:1]
	s_cbranch_vccnz .LBB0_381

;     __device__ bool next(int i, Unit& u) const { if (!base.next(i >> 1, u)) return false; if (i & 1) { u.pm += MTOK / BM; u.pn += DM / BM; } return true; }
;   __device__ __forceinline__ bool next(int i,AttnUnit&u)const{ if(i>=2||vcu>=256)return false; const int s=vcu&3; u.bh=vcu>>2; u.qb=(i==0)?7-s:s; return true; }
;     __host__ __device__ bool next(int i, Unit& u) const {
;         const int L = i * G + c; if (L >= nwg) return false;
;         int wgid = L; { const int q = nwg / NXCD, r = nwg % NXCD, xcd = wgid % NXCD, off = wgid / NXCD; wgid = (xcd < r ? xcd * (q + 1) : r * (q + 1) + (xcd - r) * q) + off; }
;         const int nig = WGM * nN, gid = wgid / nig, fm = gid * WGM, gsz = (nM - fm) < WGM ? (nM - fm) : WGM;
;         u.pm = fm + ((wgid % nig) % gsz); u.pn = (wgid % nig) / gsz; u.half = 0; return true;
; template <class Epi, class Sched, bool ALIGN_EPI = false, bool SP2 = false>
; __device__ __forceinline__ void gemm_phase(PG8_LAS unsigned char* lds, const Gemm g, const Sched& S, const Epi& E) {
;     ...
;         const bool has_next = S.next(ui + 1, nxt);
;         const char* nA = has_next ? (const char*)g.A + (size_t)nxt.pm * tstep + (nxt.half == 2 ? hstep : (size_t)0) : cA; const char* nB = has_next ? (const char*)g.Bt + (size_t)nxt.pn * tstep : cB;
.LBB0_392:
	s_add_i32 s72, s72, 1
	s_mul_i32 s10, s72, s33
	s_add_i32 s10, s10, s21
	s_cmpk_lt_i32 s10, 0x480
	s_cselect_b64 s[64:65], -1, 0
	s_cmpk_gt_i32 s10, 0x47f
	s_cbranch_scc1 .LBB0_394
	s_ashr_i32 s11, s10, 31
	s_lshr_b32 s11, s11, 29
	s_add_i32 s11, s10, s11
	s_ashr_i32 s12, s11, 3
	s_and_b32 s11, s11, -8
	s_sub_i32 s10, s10, s11
	s_cmp_lt_i32 s10, 0
	s_movk_i32 s11, 0x91
	s_cselect_b32 s11, s11, 0x90
	s_mul_i32 s10, s10, s11
	s_add_i32 s10, s10, s12
	s_mul_hi_i32 s11, s10, 0x38e38e39
	s_lshr_b32 s12, s11, 31
	s_ashr_i32 s11, s11, 5
	s_add_i32 s11, s11, s12
	s_lshl_b32 s12, s11, 3
	s_mulk_i32 s11, 0x90
	s_sub_i32 s10, s10, s11
	s_bfe_u32 s11, s10, 0x3001c
	s_add_i32 s11, s10, s11
	s_sext_i32_i16 s13, s11
	s_and_b32 s11, s11, 0xfff8
	s_sub_i32 s10, s10, s11
	s_sext_i32_i16 s10, s10
	s_add_i32 s60, s12, s10
	s_ashr_i32 s62, s13, 3
	s_mul_i32 s10, s62, 5
	s_cmp_lt_u32 s62, 12
	s_cbranch_scc0 .Lpn_hi1
	s_mov_b32 s12, 0x8e5080c4
	s_mov_b32 s13, 0x8392818
	s_branch .Lpn_go1
.Lpn_hi1:
	s_sub_i32 s10, s10, 60
	s_mov_b32 s12, 0x1ab8bd8a
	s_mov_b32 s13, 0
.Lpn_go1:
	s_lshr_b64 s[12:13], s[12:13], s10
	s_and_b32 s62, s12, 31
